# priorities: indexer pass 2, select stage (threshold/collect/descent/compaction) 1, attention and row/hist stage 0
# speedup vs baseline: 1.0037x; 1.0037x over previous
.LBB0_706:
	s_or_b64 exec, exec, s[0:1]
	s_lshl_b32 s2, s16, 2
	s_andn2_b32 s2, s2, 31
	s_and_b32 s0, s16, 7
	s_and_b32 s1, s13, 1
	s_xor_b32 s6, s2, 0x3e0
	s_cmp_eq_u32 s1, 0
	s_cselect_b32 s1, s2, s6
	s_sub_i32 s6, 0x1fe0, s1
	s_lshl_b32 s25, s0, 13
	s_add_i32 s8, s6, s25
	s_lshl_b32 s2, s0, 20
	s_ashr_i32 s9, s8, 31
	s_ashr_i32 s7, s6, 5
	v_readlane_b32 s0, v254, 49
	s_add_u32 s0, s0, s2
	v_readlane_b32 s1, v254, 50
	s_addc_u32 s1, s1, 0
	s_lshl_b64 s[10:11], s[8:9], 5
	v_lshl_add_u64 v[2:3], v[146:147], 0, s[10:11]
	global_load_dwordx4 v[66:69], v[2:3], off
	global_load_dwordx4 v[70:73], v[2:3], off offset:16
	s_lshl_b64 s[8:9], s[8:9], 10
	v_lshl_add_u64 v[62:63], v[144:145], 0, s[8:9]
	global_load_dwordx4 v[2:5], v[62:63], off
	global_load_dwordx4 v[6:9], v[62:63], off offset:128
	global_load_dwordx4 v[10:13], v[62:63], off offset:256
	global_load_dwordx4 v[14:17], v[62:63], off offset:384
	global_load_dwordx4 v[18:21], v[62:63], off offset:512
	global_load_dwordx4 v[22:25], v[62:63], off offset:640
	global_load_dwordx4 v[26:29], v[62:63], off offset:768
	global_load_dwordx4 v[30:33], v[62:63], off offset:896
	global_load_dwordx4 v[34:37], v[62:63], off offset:64
	global_load_dwordx4 v[38:41], v[62:63], off offset:192
	global_load_dwordx4 v[42:45], v[62:63], off offset:320
	global_load_dwordx4 v[46:49], v[62:63], off offset:448
	global_load_dwordx4 v[50:53], v[62:63], off offset:576
	global_load_dwordx4 v[54:57], v[62:63], off offset:704
	global_load_dwordx4 v[58:61], v[62:63], off offset:832
	s_nop 0
	global_load_dwordx4 v[62:65], v[62:63], off offset:960
	v_lshl_add_u64 v[184:185], s[0:1], 0, v[152:153]
	v_lshl_add_u64 v[184:185], v[184:185], 0, v[154:155]
	s_mov_b64 s[10:11], 0x800
	v_lshl_add_u64 v[186:187], v[184:185], 0, s[10:11]
	global_load_dwordx4 v[134:137], v[184:185], off
	global_load_dwordx4 v[130:133], v[184:185], off offset:1024
	s_mov_b64 s[10:11], 0x1000
	v_lshl_add_u64 v[188:189], v[184:185], 0, s[10:11]
	global_load_dwordx4 v[126:129], v[186:187], off
	global_load_dwordx4 v[122:125], v[186:187], off offset:1024
	s_mov_b64 s[10:11], 0x1800
	v_lshl_add_u64 v[184:185], v[184:185], 0, s[10:11]
	global_load_dwordx4 v[110:113], v[188:189], off
	global_load_dwordx4 v[106:109], v[188:189], off offset:1024
	global_load_dwordx4 v[94:97], v[184:185], off
	global_load_dwordx4 v[90:93], v[184:185], off offset:1024
	s_add_i32 s7, s7, 1
	s_ashr_i32 s9, s6, 4
	s_lshl_b32 s8, s7, 1
	v_lshl_add_u64 v[172:173], s[0:1], 0, v[154:155]
	s_waitcnt lgkmcnt(0)
	s_barrier
	s_waitcnt vmcnt(23)
	v_and_b32_e32 v83, 0xffff0000, v3
	v_lshlrev_b32_e32 v82, 16, v3
	s_waitcnt vmcnt(22)
	v_and_b32_e32 v85, 0xffff0000, v7
	v_mul_f32_e32 v156, 0.5, v66
	v_mul_f32_e32 v158, 0.5, v67
	v_and_b32_e32 v67, 0xffff0000, v2
	v_lshlrev_b32_e32 v66, 16, v2
	v_mul_f32_e32 v160, 0.5, v68
	v_mul_f32_e32 v162, 0.5, v69
	v_and_b32_e32 v69, 0xffff0000, v6
	v_lshlrev_b32_e32 v68, 16, v6
	v_lshlrev_b32_e32 v84, 16, v7
	v_pk_fma_f32 v[66:67], v[156:157], v[66:67], 0 op_sel_hi:[0,1,0]
	v_pk_fma_f32 v[82:83], v[156:157], v[82:83], 0 op_sel_hi:[0,1,0]
	v_mul_f32_e32 v164, 0.5, v70
	v_mul_f32_e32 v166, 0.5, v71
	s_waitcnt vmcnt(21)
	v_and_b32_e32 v71, 0xffff0000, v10
	v_lshlrev_b32_e32 v70, 16, v10
	v_and_b32_e32 v87, 0xffff0000, v11
	v_lshlrev_b32_e32 v86, 16, v11
	v_pk_fma_f32 v[66:67], v[158:159], v[68:69], v[66:67] op_sel_hi:[0,1,1]
	v_pk_fma_f32 v[68:69], v[158:159], v[84:85], v[82:83] op_sel_hi:[0,1,1]
	v_mul_f32_e32 v168, 0.5, v72
	v_mul_f32_e32 v170, 0.5, v73
	s_waitcnt vmcnt(20)
	v_and_b32_e32 v73, 0xffff0000, v14
	v_lshlrev_b32_e32 v72, 16, v14
	v_and_b32_e32 v89, 0xffff0000, v15
	v_lshlrev_b32_e32 v88, 16, v15
	v_pk_fma_f32 v[66:67], v[160:161], v[70:71], v[66:67] op_sel_hi:[0,1,1]
	v_pk_fma_f32 v[68:69], v[160:161], v[86:87], v[68:69] op_sel_hi:[0,1,1]
	s_waitcnt vmcnt(19)
	v_and_b32_e32 v75, 0xffff0000, v18
	v_lshlrev_b32_e32 v74, 16, v18
	v_and_b32_e32 v177, 0xffff0000, v19
	v_lshlrev_b32_e32 v176, 16, v19
	v_pk_fma_f32 v[66:67], v[162:163], v[72:73], v[66:67] op_sel_hi:[0,1,1]
	v_pk_fma_f32 v[68:69], v[162:163], v[88:89], v[68:69] op_sel_hi:[0,1,1]
	s_waitcnt vmcnt(18)
	v_and_b32_e32 v77, 0xffff0000, v22
	v_lshlrev_b32_e32 v76, 16, v22
	v_and_b32_e32 v179, 0xffff0000, v23
	v_lshlrev_b32_e32 v178, 16, v23
	v_pk_fma_f32 v[66:67], v[164:165], v[74:75], v[66:67] op_sel_hi:[0,1,1]
	v_pk_fma_f32 v[68:69], v[164:165], v[176:177], v[68:69] op_sel_hi:[0,1,1]
	s_waitcnt vmcnt(17)
	v_and_b32_e32 v79, 0xffff0000, v26
	v_lshlrev_b32_e32 v78, 16, v26
	v_and_b32_e32 v181, 0xffff0000, v27
	v_lshlrev_b32_e32 v180, 16, v27
	v_pk_fma_f32 v[66:67], v[166:167], v[76:77], v[66:67] op_sel_hi:[0,1,1]
	v_pk_fma_f32 v[68:69], v[166:167], v[178:179], v[68:69] op_sel_hi:[0,1,1]
	s_waitcnt vmcnt(16)
	v_and_b32_e32 v81, 0xffff0000, v30
	v_lshlrev_b32_e32 v80, 16, v30
	v_and_b32_e32 v183, 0xffff0000, v31
	v_lshlrev_b32_e32 v182, 16, v31
	v_pk_fma_f32 v[66:67], v[168:169], v[78:79], v[66:67] op_sel_hi:[0,1,1]
	v_pk_fma_f32 v[68:69], v[168:169], v[180:181], v[68:69] op_sel_hi:[0,1,1]
	v_and_b32_e32 v99, 0xffff0000, v4
	v_lshlrev_b32_e32 v98, 16, v4
	v_pk_fma_f32 v[66:67], v[170:171], v[80:81], v[66:67] op_sel_hi:[0,1,1]
	v_pk_fma_f32 v[68:69], v[170:171], v[182:183], v[68:69] op_sel_hi:[0,1,1]
	v_cvt_pk_bf16_f32 v66, v66, v67
	v_cvt_pk_bf16_f32 v67, v68, v69
	v_pk_fma_f32 v[68:69], v[156:157], v[98:99], 0 op_sel_hi:[0,1,0]
	v_and_b32_e32 v71, 0xffff0000, v8
	v_lshlrev_b32_e32 v70, 16, v8
	v_pk_fma_f32 v[68:69], v[158:159], v[70:71], v[68:69] op_sel_hi:[0,1,1]
	v_and_b32_e32 v71, 0xffff0000, v12
	v_lshlrev_b32_e32 v70, 16, v12
	v_pk_fma_f32 v[68:69], v[160:161], v[70:71], v[68:69] op_sel_hi:[0,1,1]
	v_and_b32_e32 v71, 0xffff0000, v16
	v_lshlrev_b32_e32 v70, 16, v16
	v_pk_fma_f32 v[68:69], v[162:163], v[70:71], v[68:69] op_sel_hi:[0,1,1]
	v_and_b32_e32 v71, 0xffff0000, v20
	v_lshlrev_b32_e32 v70, 16, v20
	v_pk_fma_f32 v[68:69], v[164:165], v[70:71], v[68:69] op_sel_hi:[0,1,1]
	v_and_b32_e32 v71, 0xffff0000, v24
	v_lshlrev_b32_e32 v70, 16, v24
	v_pk_fma_f32 v[68:69], v[166:167], v[70:71], v[68:69] op_sel_hi:[0,1,1]
	v_and_b32_e32 v71, 0xffff0000, v28
	v_lshlrev_b32_e32 v70, 16, v28
	v_pk_fma_f32 v[68:69], v[168:169], v[70:71], v[68:69] op_sel_hi:[0,1,1]
	v_and_b32_e32 v71, 0xffff0000, v32
	v_lshlrev_b32_e32 v70, 16, v32
	v_pk_fma_f32 v[68:69], v[170:171], v[70:71], v[68:69] op_sel_hi:[0,1,1]
	v_and_b32_e32 v71, 0xffff0000, v5
	v_lshlrev_b32_e32 v70, 16, v5
	v_pk_fma_f32 v[70:71], v[156:157], v[70:71], 0 op_sel_hi:[0,1,0]
	v_and_b32_e32 v73, 0xffff0000, v9
	v_lshlrev_b32_e32 v72, 16, v9
	v_pk_fma_f32 v[70:71], v[158:159], v[72:73], v[70:71] op_sel_hi:[0,1,1]
	v_and_b32_e32 v73, 0xffff0000, v13
	v_lshlrev_b32_e32 v72, 16, v13
	v_pk_fma_f32 v[70:71], v[160:161], v[72:73], v[70:71] op_sel_hi:[0,1,1]
	v_and_b32_e32 v73, 0xffff0000, v17
	v_lshlrev_b32_e32 v72, 16, v17
	v_pk_fma_f32 v[70:71], v[162:163], v[72:73], v[70:71] op_sel_hi:[0,1,1]
	v_and_b32_e32 v73, 0xffff0000, v21
	v_lshlrev_b32_e32 v72, 16, v21
	v_pk_fma_f32 v[70:71], v[164:165], v[72:73], v[70:71] op_sel_hi:[0,1,1]
	v_and_b32_e32 v73, 0xffff0000, v25
	v_lshlrev_b32_e32 v72, 16, v25
	v_pk_fma_f32 v[70:71], v[166:167], v[72:73], v[70:71] op_sel_hi:[0,1,1]
	v_and_b32_e32 v73, 0xffff0000, v29
	v_lshlrev_b32_e32 v72, 16, v29
	v_pk_fma_f32 v[70:71], v[168:169], v[72:73], v[70:71] op_sel_hi:[0,1,1]
	v_and_b32_e32 v73, 0xffff0000, v33
	v_lshlrev_b32_e32 v72, 16, v33
	v_pk_fma_f32 v[70:71], v[170:171], v[72:73], v[70:71] op_sel_hi:[0,1,1]
	v_cvt_pk_bf16_f32 v68, v68, v69
	v_cvt_pk_bf16_f32 v69, v70, v71
	s_waitcnt vmcnt(15)
	v_and_b32_e32 v71, 0xffff0000, v34
	v_lshlrev_b32_e32 v70, 16, v34
	v_pk_fma_f32 v[70:71], v[156:157], v[70:71], 0 op_sel_hi:[0,1,0]
	s_waitcnt vmcnt(14)
	v_and_b32_e32 v73, 0xffff0000, v38
	v_lshlrev_b32_e32 v72, 16, v38
	v_pk_fma_f32 v[70:71], v[158:159], v[72:73], v[70:71] op_sel_hi:[0,1,1]
	s_waitcnt vmcnt(13)
	v_and_b32_e32 v73, 0xffff0000, v42
	v_lshlrev_b32_e32 v72, 16, v42
	v_pk_fma_f32 v[70:71], v[160:161], v[72:73], v[70:71] op_sel_hi:[0,1,1]
	s_waitcnt vmcnt(12)
	v_and_b32_e32 v73, 0xffff0000, v46
	v_lshlrev_b32_e32 v72, 16, v46
	v_pk_fma_f32 v[70:71], v[162:163], v[72:73], v[70:71] op_sel_hi:[0,1,1]
	s_waitcnt vmcnt(11)
	v_and_b32_e32 v73, 0xffff0000, v50
	v_lshlrev_b32_e32 v72, 16, v50
	v_pk_fma_f32 v[70:71], v[164:165], v[72:73], v[70:71] op_sel_hi:[0,1,1]
	s_waitcnt vmcnt(10)
	v_and_b32_e32 v73, 0xffff0000, v54
	v_lshlrev_b32_e32 v72, 16, v54
	v_pk_fma_f32 v[70:71], v[166:167], v[72:73], v[70:71] op_sel_hi:[0,1,1]
	s_waitcnt vmcnt(9)
	v_and_b32_e32 v73, 0xffff0000, v58
	v_lshlrev_b32_e32 v72, 16, v58
	v_pk_fma_f32 v[70:71], v[168:169], v[72:73], v[70:71] op_sel_hi:[0,1,1]
	s_waitcnt vmcnt(8)
	v_and_b32_e32 v73, 0xffff0000, v62
	v_lshlrev_b32_e32 v72, 16, v62
	v_pk_fma_f32 v[70:71], v[170:171], v[72:73], v[70:71] op_sel_hi:[0,1,1]
	v_and_b32_e32 v73, 0xffff0000, v35
	v_lshlrev_b32_e32 v72, 16, v35
	v_pk_fma_f32 v[72:73], v[156:157], v[72:73], 0 op_sel_hi:[0,1,0]
	v_and_b32_e32 v75, 0xffff0000, v39
	v_lshlrev_b32_e32 v74, 16, v39
	v_pk_fma_f32 v[72:73], v[158:159], v[74:75], v[72:73] op_sel_hi:[0,1,1]
	v_and_b32_e32 v75, 0xffff0000, v43
	v_lshlrev_b32_e32 v74, 16, v43
	v_pk_fma_f32 v[72:73], v[160:161], v[74:75], v[72:73] op_sel_hi:[0,1,1]
	v_and_b32_e32 v75, 0xffff0000, v47
	v_lshlrev_b32_e32 v74, 16, v47
	v_pk_fma_f32 v[72:73], v[162:163], v[74:75], v[72:73] op_sel_hi:[0,1,1]
	v_and_b32_e32 v75, 0xffff0000, v51
	v_lshlrev_b32_e32 v74, 16, v51
	v_pk_fma_f32 v[72:73], v[164:165], v[74:75], v[72:73] op_sel_hi:[0,1,1]
	v_and_b32_e32 v75, 0xffff0000, v55
	v_lshlrev_b32_e32 v74, 16, v55
	v_pk_fma_f32 v[72:73], v[166:167], v[74:75], v[72:73] op_sel_hi:[0,1,1]
	v_and_b32_e32 v75, 0xffff0000, v59
	v_lshlrev_b32_e32 v74, 16, v59
	v_pk_fma_f32 v[72:73], v[168:169], v[74:75], v[72:73] op_sel_hi:[0,1,1]
	v_and_b32_e32 v75, 0xffff0000, v63
	v_lshlrev_b32_e32 v74, 16, v63
	v_pk_fma_f32 v[72:73], v[170:171], v[74:75], v[72:73] op_sel_hi:[0,1,1]
	v_cvt_pk_bf16_f32 v70, v70, v71
	v_cvt_pk_bf16_f32 v71, v72, v73
	v_and_b32_e32 v73, 0xffff0000, v36
	v_lshlrev_b32_e32 v72, 16, v36
	v_pk_fma_f32 v[72:73], v[156:157], v[72:73], 0 op_sel_hi:[0,1,0]
	v_and_b32_e32 v75, 0xffff0000, v40
	v_lshlrev_b32_e32 v74, 16, v40
	v_pk_fma_f32 v[72:73], v[158:159], v[74:75], v[72:73] op_sel_hi:[0,1,1]
	v_and_b32_e32 v75, 0xffff0000, v44
	v_lshlrev_b32_e32 v74, 16, v44
	v_pk_fma_f32 v[72:73], v[160:161], v[74:75], v[72:73] op_sel_hi:[0,1,1]
	v_and_b32_e32 v75, 0xffff0000, v48
	v_lshlrev_b32_e32 v74, 16, v48
	v_pk_fma_f32 v[72:73], v[162:163], v[74:75], v[72:73] op_sel_hi:[0,1,1]
	v_and_b32_e32 v75, 0xffff0000, v52
	v_lshlrev_b32_e32 v74, 16, v52
	v_pk_fma_f32 v[72:73], v[164:165], v[74:75], v[72:73] op_sel_hi:[0,1,1]
	v_and_b32_e32 v75, 0xffff0000, v56
	v_lshlrev_b32_e32 v74, 16, v56
	v_pk_fma_f32 v[72:73], v[166:167], v[74:75], v[72:73] op_sel_hi:[0,1,1]
	v_and_b32_e32 v75, 0xffff0000, v60
	v_lshlrev_b32_e32 v74, 16, v60
	v_pk_fma_f32 v[72:73], v[168:169], v[74:75], v[72:73] op_sel_hi:[0,1,1]
	v_and_b32_e32 v75, 0xffff0000, v64
	v_lshlrev_b32_e32 v74, 16, v64
	v_pk_fma_f32 v[72:73], v[170:171], v[74:75], v[72:73] op_sel_hi:[0,1,1]
	v_and_b32_e32 v75, 0xffff0000, v37
	v_lshlrev_b32_e32 v74, 16, v37
	v_pk_fma_f32 v[74:75], v[156:157], v[74:75], 0 op_sel_hi:[0,1,0]
	v_and_b32_e32 v77, 0xffff0000, v41
	v_lshlrev_b32_e32 v76, 16, v41
	v_pk_fma_f32 v[74:75], v[158:159], v[76:77], v[74:75] op_sel_hi:[0,1,1]
	v_and_b32_e32 v77, 0xffff0000, v45
	v_lshlrev_b32_e32 v76, 16, v45
	v_pk_fma_f32 v[74:75], v[160:161], v[76:77], v[74:75] op_sel_hi:[0,1,1]
	v_and_b32_e32 v77, 0xffff0000, v49
	v_lshlrev_b32_e32 v76, 16, v49
	v_pk_fma_f32 v[74:75], v[162:163], v[76:77], v[74:75] op_sel_hi:[0,1,1]
	v_and_b32_e32 v77, 0xffff0000, v53
	v_lshlrev_b32_e32 v76, 16, v53
	v_pk_fma_f32 v[74:75], v[164:165], v[76:77], v[74:75] op_sel_hi:[0,1,1]
	v_and_b32_e32 v77, 0xffff0000, v57
	v_lshlrev_b32_e32 v76, 16, v57
	v_pk_fma_f32 v[74:75], v[166:167], v[76:77], v[74:75] op_sel_hi:[0,1,1]
	v_and_b32_e32 v77, 0xffff0000, v61
	v_lshlrev_b32_e32 v76, 16, v61
	v_pk_fma_f32 v[74:75], v[168:169], v[76:77], v[74:75] op_sel_hi:[0,1,1]
	v_and_b32_e32 v77, 0xffff0000, v65
	v_lshlrev_b32_e32 v76, 16, v65
	v_pk_fma_f32 v[74:75], v[170:171], v[76:77], v[74:75] op_sel_hi:[0,1,1]
	v_cvt_pk_bf16_f32 v72, v72, v73
	v_cvt_pk_bf16_f32 v73, v74, v75
	v_readlane_b32 s10, v254, 53
	s_waitcnt vmcnt(0)
	s_add_i32 s9, s10, s9
	s_min_i32 s9, s8, s9
	s_cmp_ge_i32 s12, s9
	s_cbranch_scc1 .LBB0_709
	v_readfirstlane_b32 s0, v138
	s_nop 3
	s_cmp_lt_u32 s0, 16
	s_cbranch_scc1 .Lstagger_skip
	s_sleep 55
	s_setprio 2

.Lmk_done:
	v_readlane_b32 s8, v255, 19
	s_cmpk_lt_i32 s97, 0x100
	s_cbranch_scc1 .LBB0_759
	s_setprio 1
	s_lshl_b32 s0, s0, 11
	s_add_i32 s0, s0, 0
	s_mov_b32 s83, s78
	s_mov_b32 s77, s76
	s_mov_b32 s75, s74
	s_waitcnt lgkmcnt(1)
	v_add_u32_e32 v78, v2, v3
	v_add3_u32 v78, v78, v5, v4
	s_waitcnt lgkmcnt(0)
	v_add3_u32 v78, v78, v9, v8
	s_mov_b32 s73, s72
	s_mov_b32 s72, s70
	s_mov_b32 s76, s65
	s_mov_b32 s74, s63
	s_mov_b32 s69, s62
	s_mov_b32 s68, s58
	s_mov_b32 s66, s56
	s_mov_b32 s65, s55
	s_mov_b32 s64, s6
	s_mov_b32 s6, s51
	s_mov_b32 s58, s50
	s_mov_b64 s[62:63], s[48:49]
	s_mov_b32 s56, s43
	s_mov_b32 s49, s42
	s_mov_b32 s48, s41
	s_mov_b32 s91, s40
	s_mov_b32 s90, s39
	s_mov_b32 s89, s38
	s_mov_b32 s88, s2
	s_mov_b32 s2, s37
	s_mov_b32 s84, s7
	s_mov_b32 s7, s36
	s_mov_b32 s85, s35
	s_mov_b32 s44, s34
	s_mov_b32 s51, s31
	s_mov_b32 s50, s30
	s_mov_b32 s92, s29
	s_mov_b32 s71, s28
	s_mov_b32 s70, s27
	s_mov_b32 s81, s26
	s_mov_b32 s82, s25
	s_mov_b32 s55, s22
	v_add3_u32 v78, v78, v7, v6
	s_mov_b32 s9, 63
	s_nop 0
	v_readlane_b32 s25, v78, 63
	v_readlane_b32 s26, v78, 62
	v_readlane_b32 s27, v78, 61
	v_readlane_b32 s28, v78, 60
	v_readlane_b32 s29, v78, 59
	v_readlane_b32 s30, v78, 58
	v_readlane_b32 s31, v78, 57
	v_readlane_b32 s34, v78, 56
	v_readlane_b32 s35, v78, 55
	v_readlane_b32 s36, v78, 54
	v_readlane_b32 s37, v78, 53
	v_readlane_b32 s38, v78, 52
	v_readlane_b32 s39, v78, 51
	v_readlane_b32 s40, v78, 50
	v_readlane_b32 s41, v78, 49
	v_readlane_b32 s42, v78, 48
	s_mov_b32 s8, s1
	s_add_i32 s1, s8, s25
	s_cmpk_gt_u32 s1, 0xff
	s_cbranch_scc1 .Lthr_f63
	s_mov_b32 s8, s1
	s_add_i32 s1, s8, s26
	s_cmpk_gt_u32 s1, 0xff
	s_cbranch_scc1 .Lthr_f62
	s_mov_b32 s8, s1
	s_add_i32 s1, s8, s27
	s_cmpk_gt_u32 s1, 0xff
	s_cbranch_scc1 .Lthr_f61
	s_mov_b32 s8, s1
	s_add_i32 s1, s8, s28
	s_cmpk_gt_u32 s1, 0xff
	s_cbranch_scc1 .Lthr_f60
	s_mov_b32 s8, s1
	s_add_i32 s1, s8, s29
	s_cmpk_gt_u32 s1, 0xff
	s_cbranch_scc1 .Lthr_f59
	s_mov_b32 s8, s1
	s_add_i32 s1, s8, s30
	s_cmpk_gt_u32 s1, 0xff
	s_cbranch_scc1 .Lthr_f58
	s_mov_b32 s8, s1
	s_add_i32 s1, s8, s31
	s_cmpk_gt_u32 s1, 0xff
	s_cbranch_scc1 .Lthr_f57
	s_mov_b32 s8, s1
	s_add_i32 s1, s8, s34
	s_cmpk_gt_u32 s1, 0xff
	s_cbranch_scc1 .Lthr_f56
	s_mov_b32 s8, s1
	s_add_i32 s1, s8, s35
	s_cmpk_gt_u32 s1, 0xff
	s_cbranch_scc1 .Lthr_f55
	s_mov_b32 s8, s1
	s_add_i32 s1, s8, s36
	s_cmpk_gt_u32 s1, 0xff
	s_cbranch_scc1 .Lthr_f54
	s_mov_b32 s8, s1
	s_add_i32 s1, s8, s37
	s_cmpk_gt_u32 s1, 0xff
	s_cbranch_scc1 .Lthr_f53
	s_mov_b32 s8, s1
	s_add_i32 s1, s8, s38
	s_cmpk_gt_u32 s1, 0xff
	s_cbranch_scc1 .Lthr_f52
	s_mov_b32 s8, s1
	s_add_i32 s1, s8, s39
	s_cmpk_gt_u32 s1, 0xff
	s_cbranch_scc1 .Lthr_f51
	s_mov_b32 s8, s1
	s_add_i32 s1, s8, s40
	s_cmpk_gt_u32 s1, 0xff
	s_cbranch_scc1 .Lthr_f50
	s_mov_b32 s8, s1
	s_add_i32 s1, s8, s41
	s_cmpk_gt_u32 s1, 0xff
	s_cbranch_scc1 .Lthr_f49
	s_mov_b32 s8, s1
	s_add_i32 s1, s8, s42
	s_cmpk_gt_u32 s1, 0xff
	s_cbranch_scc1 .Lthr_f48
	s_mov_b32 s8, s1
	s_mov_b32 s9, 47
	s_branch .LBB0_723

.LBB0_921:
	s_setprio 0
	v_readlane_b32 s46, v255, 35
	s_mov_b32 s22, s55
	s_mov_b32 s23, 0xff800000
	s_movk_i32 s24, 0x50
	s_mov_b32 s25, s82
	s_mov_b32 s26, s81
	s_mov_b32 s27, s70
	s_mov_b32 s28, s71
	s_mov_b32 s29, s92
	s_mov_b32 s30, s50
	s_mov_b32 s31, s51
	s_mov_b32 s34, s44
	s_mov_b32 s35, s85
	s_mov_b32 s36, s7
	s_mov_b32 s7, s84
	s_mov_b32 s37, s2
	s_mov_b32 s2, s88
	s_mov_b32 s38, s89
	s_mov_b32 s39, s90
	s_mov_b32 s40, s91
	s_mov_b32 s41, s48
	s_mov_b32 s42, s49
	s_mov_b32 s43, s56
	v_readlane_b32 s44, v255, 45
	v_readlane_b32 s47, v255, 36
	s_mov_b64 s[48:49], s[62:63]
	s_mov_b32 s50, s58
	s_mov_b32 s51, s6
	s_mov_b32 s6, s64
	s_mov_b32 s55, s65
	s_mov_b32 s56, s66
	s_mov_b32 s58, s68
	s_mov_b32 s62, s69
	s_mov_b32 s63, s74
	v_readlane_b32 s64, v255, 39
	s_mov_b32 s65, s76
	v_readlane_b32 s66, v255, 41
	v_readlane_b32 s68, v255, 43
	v_readlane_b32 s69, v255, 34
	s_mov_b32 s70, s72
	v_readlane_b32 s71, v255, 37
	s_mov_b32 s72, s73
	v_readlane_b32 s73, v255, 38
	s_mov_b32 s74, s75
	v_readlane_b32 s75, v255, 40
	s_mov_b32 s76, s77
	v_readlane_b32 s77, v255, 42
	s_mov_b32 s78, s83
	v_readlane_b32 s79, v255, 44
	v_readlane_b32 s82, v255, 46
	v_readlane_b32 s83, v255, 47
	v_readlane_b32 s84, v255, 48
	v_readlane_b32 s85, v255, 49
	v_readlane_b32 s86, v255, 50
	v_readlane_b32 s87, v255, 51
	v_readlane_b32 s88, v255, 52
	v_readlane_b32 s89, v255, 53
	v_readlane_b32 s90, v255, 54
	v_readlane_b32 s91, v255, 55
	v_readlane_b32 s92, v255, 56
	v_readlane_b32 s94, v255, 57
	s_and_b64 vcc, exec, s[0:1]
	s_cbranch_vccnz .LBB0_1194
